# code placement: 4-byte pads at six barrier sites so every compiler loop head sits at the baseline's byte phase mod 8
# baseline (speedup 1.0000x reference)
.Lcwarm_s:
	s_nop 0
	v_writelane_b32 v253, s12, 10
	s_load_dwordx16 s[36:51], s[0:1], 0x80
	s_add_u32 s2, s88, 0x80000
	v_writelane_b32 v253, s13, 11
	s_addc_u32 s3, s89, 0
	v_writelane_b32 v253, s2, 12
	v_cmp_eq_u32_e64 s[4:5], 0, v236
	s_nop 0
	v_writelane_b32 v253, s3, 13
	s_getreg_b32 s2, hwreg(HW_REG_XCC_ID, 0, 4)
	s_and_b32 s2, s2, 15
	v_writelane_b32 v253, s2, 14
	s_mov_b64 s[2:3], exec
	v_writelane_b32 v253, s4, 15
	s_nop 1
	v_writelane_b32 v253, s5, 16
	s_and_b64 s[4:5], s[2:3], s[4:5]
	s_mov_b64 exec, s[4:5]
	s_cbranch_execz .LBB0_17
	s_mov_b64 s[4:5], exec
	v_mbcnt_lo_u32_b32 v0, s4, 0
	v_mbcnt_hi_u32_b32 v0, s5, v0
	v_cmp_eq_u32_e32 vcc, 0, v0
	s_and_b64 s[6:7], exec, vcc
	s_mov_b64 exec, s[6:7]
	s_cbranch_execz .LBB0_17
	v_readlane_b32 s6, v253, 14
	s_bcnt1_i32_b64 s4, s[4:5]
	s_lshl_b32 s6, s6, 8
	v_mov_b32_e32 v1, s4
	v_readlane_b32 s4, v253, 12
	v_mov_b32_e32 v0, s6
	v_readlane_b32 s5, v253, 13
	s_nop 4
	global_atomic_add v0, v1, s[4:5] offset:1024

.Lcwarm_0:
	s_nop 0
	s_mov_b64 s[0:1], exec
	v_readlane_b32 s4, v253, 15
	v_readlane_b32 s5, v253, 16
	s_and_b64 s[4:5], s[0:1], s[4:5]
	s_mov_b64 exec, s[4:5]
	s_cbranch_execz .LBB0_112
	s_add_i32 s4, 0, 0x27fc0
	v_mov_b32_e32 v0, s4
	s_waitcnt vmcnt(0) expcnt(0) lgkmcnt(0)
	ds_read_b32 v2, v0
	s_add_i32 s4, 0, 0x27fc4
	v_mov_b32_e32 v0, s4
	ds_read_b32 v0, v0
	s_waitcnt lgkmcnt(1)
	v_cmp_ne_u32_e32 vcc, 0, v2
	s_cbranch_vccnz .LBB0_76
	v_readlane_b32 s4, v253, 10
	v_readlane_b32 s5, v253, 11
	v_readlane_b32 s6, v253, 8
	s_mul_i32 s31, s5, s6
	s_mul_i32 s31, s31, s4
	s_add_u32 s4, s88, 0x80200
	s_addc_u32 s5, s89, 0
	s_add_u32 s6, s88, 0x80400
	s_addc_u32 s7, s89, 0
	s_add_u32 s8, s88, 0x80500
	s_addc_u32 s9, s89, 0
	s_add_u32 s10, s88, 0x80600
	s_addc_u32 s11, s89, 0
	s_add_u32 s12, s88, 0x80700
	s_addc_u32 s13, s89, 0
	s_add_u32 s14, s88, 0x80800
	s_addc_u32 s15, s89, 0
	s_add_u32 s16, s88, 0x80900
	s_addc_u32 s17, s89, 0
	s_add_u32 s18, s88, 0x80a00
	s_addc_u32 s19, s89, 0
	s_add_u32 s20, s88, 0x80b00
	s_addc_u32 s21, s89, 0
	s_add_u32 s22, s88, 0x80c00
	s_addc_u32 s23, s89, 0
	s_add_u32 s24, s88, 0x80d00
	s_addc_u32 s25, s89, 0
	s_add_u32 s26, s88, 0x80e00
	s_addc_u32 s27, s89, 0
	s_add_u32 s28, s88, 0x80f00
	s_addc_u32 s29, s89, 0
	s_add_u32 s34, s88, 0x81000
	s_addc_u32 s35, s89, 0
	s_add_u32 s40, s88, 0x81100
	s_addc_u32 s41, s89, 0
	s_add_u32 s44, s88, 0x81200
	s_addc_u32 s45, s89, 0
	s_add_u32 s52, s88, 0x81300
	s_addc_u32 s53, s89, 0
	s_mov_b32 s33, 1
	v_mov_b32_e32 v16, 0
	s_branch .LBB0_64

.Lcwarm_3:
	s_nop 0
	s_mov_b64 s[0:1], exec
	v_readlane_b32 s4, v253, 15
	v_readlane_b32 s5, v253, 16
	s_and_b64 s[4:5], s[0:1], s[4:5]
	s_mov_b64 exec, s[4:5]
	s_cbranch_execz .LBB0_509
	s_add_i32 s4, 0, 0x27fc0
	s_waitcnt vmcnt(37)
	v_mov_b32_e32 v0, s4
	s_waitcnt vmcnt(0) expcnt(0) lgkmcnt(0)
	ds_read_b32 v2, v0
	s_add_i32 s4, 0, 0x27fc4
	v_mov_b32_e32 v0, s4
	ds_read_b32 v0, v0
	s_waitcnt lgkmcnt(1)
	v_cmp_ne_u32_e32 vcc, 0, v2
	s_cbranch_vccnz .LBB0_473
	v_readlane_b32 s4, v253, 8
	s_mul_i32 s31, s77, s4
	s_add_u32 s4, s88, 0x80200
	s_addc_u32 s5, s89, 0
	s_add_u32 s6, s88, 0x80400
	s_addc_u32 s7, s89, 0
	s_add_u32 s8, s88, 0x80500
	s_addc_u32 s9, s89, 0
	s_add_u32 s10, s88, 0x80600
	s_addc_u32 s11, s89, 0
	s_add_u32 s12, s88, 0x80700
	s_addc_u32 s13, s89, 0
	s_add_u32 s14, s88, 0x80800
	s_addc_u32 s15, s89, 0
	s_add_u32 s16, s88, 0x80900
	s_addc_u32 s17, s89, 0
	s_add_u32 s18, s88, 0x80a00
	s_addc_u32 s19, s89, 0
	s_add_u32 s20, s88, 0x80b00
	s_addc_u32 s21, s89, 0
	s_add_u32 s22, s88, 0x80c00
	s_addc_u32 s23, s89, 0
	s_add_u32 s24, s88, 0x80d00
	s_addc_u32 s25, s89, 0
	s_add_u32 s26, s88, 0x80e00
	s_addc_u32 s27, s89, 0
	s_add_u32 s28, s88, 0x80f00
	s_addc_u32 s29, s89, 0
	s_add_u32 s34, s88, 0x81000
	s_addc_u32 s35, s89, 0
	s_add_u32 s36, s88, 0x81100
	s_addc_u32 s37, s89, 0
	s_add_u32 s38, s88, 0x81200
	s_addc_u32 s39, s89, 0
	s_add_u32 s48, s88, 0x81300
	s_mul_i32 s31, s31, s76
	s_addc_u32 s49, s89, 0
	s_mov_b32 s33, 1
	v_mov_b32_e32 v16, 0
	s_branch .LBB0_461

.Lcwarm_8:
	s_nop 0
	s_mov_b64 s[0:1], exec
	v_readlane_b32 s4, v253, 15
	v_readlane_b32 s5, v253, 16
	s_and_b64 s[4:5], s[0:1], s[4:5]
	s_mov_b64 exec, s[4:5]
	s_cbranch_execz .LBB0_916
	s_add_i32 s4, 0, 0x27fc0
	v_mov_b32_e32 v0, s4
	s_waitcnt vmcnt(0) expcnt(0) lgkmcnt(0)
	ds_read_b32 v2, v0
	s_add_i32 s4, 0, 0x27fc4
	v_mov_b32_e32 v0, s4
	ds_read_b32 v0, v0
	s_waitcnt lgkmcnt(1)
	v_cmp_ne_u32_e32 vcc, 0, v2
	s_cbranch_vccnz .LBB0_880
	v_readlane_b32 s4, v253, 8
	s_mul_i32 s31, s77, s4
	s_add_u32 s4, s88, 0x80200
	s_addc_u32 s5, s89, 0
	s_add_u32 s8, s88, 0x80400
	s_addc_u32 s9, s89, 0
	s_add_u32 s10, s88, 0x80500
	s_addc_u32 s11, s89, 0
	s_add_u32 s12, s88, 0x80600
	s_addc_u32 s13, s89, 0
	s_add_u32 s14, s88, 0x80700
	s_addc_u32 s15, s89, 0
	s_add_u32 s16, s88, 0x80800
	s_addc_u32 s17, s89, 0
	s_add_u32 s18, s88, 0x80900
	s_addc_u32 s19, s89, 0
	s_add_u32 s20, s88, 0x80a00
	s_addc_u32 s21, s89, 0
	s_add_u32 s22, s88, 0x80b00
	s_addc_u32 s23, s89, 0
	s_add_u32 s24, s88, 0x80c00
	s_addc_u32 s25, s89, 0
	s_add_u32 s26, s88, 0x80d00
	s_addc_u32 s27, s89, 0
	s_add_u32 s28, s88, 0x80e00
	s_addc_u32 s29, s89, 0
	s_add_u32 s34, s88, 0x80f00
	s_addc_u32 s35, s89, 0
	s_add_u32 s36, s88, 0x81000
	s_addc_u32 s37, s89, 0
	s_add_u32 s38, s88, 0x81100
	s_addc_u32 s39, s89, 0
	s_add_u32 s42, s88, 0x81200
	s_addc_u32 s43, s89, 0
	s_add_u32 s44, s88, 0x81300
	s_mul_i32 s31, s31, s76
	s_addc_u32 s45, s89, 0
	s_mov_b32 s33, 1
	v_mov_b32_e32 v16, 0
	s_branch .LBB0_868

.Lcwarm_10:
	s_nop 0
	s_mov_b64 s[0:1], exec
	v_readlane_b32 s4, v253, 15
	v_readlane_b32 s5, v253, 16
	s_and_b64 s[4:5], s[0:1], s[4:5]
	s_mov_b64 exec, s[4:5]
	s_cbranch_execz .LBB0_1072
	s_add_i32 s4, 0, 0x27fc0
	v_mov_b32_e32 v0, s4
	s_waitcnt vmcnt(0) expcnt(0) lgkmcnt(0)
	ds_read_b32 v2, v0
	s_add_i32 s4, 0, 0x27fc4
	v_mov_b32_e32 v0, s4
	ds_read_b32 v0, v0
	s_waitcnt lgkmcnt(1)
	v_cmp_ne_u32_e32 vcc, 0, v2
	s_cbranch_vccnz .LBB0_1036
	v_readlane_b32 s4, v253, 8
	s_mul_i32 s31, s77, s4
	s_add_u32 s4, s88, 0x80200
	s_addc_u32 s5, s89, 0
	s_add_u32 s6, s88, 0x80400
	s_addc_u32 s7, s89, 0
	s_add_u32 s8, s88, 0x80500
	s_addc_u32 s9, s89, 0
	s_add_u32 s10, s88, 0x80600
	s_addc_u32 s11, s89, 0
	s_add_u32 s12, s88, 0x80700
	s_addc_u32 s13, s89, 0
	s_add_u32 s14, s88, 0x80800
	s_addc_u32 s15, s89, 0
	s_add_u32 s16, s88, 0x80900
	s_addc_u32 s17, s89, 0
	s_add_u32 s18, s88, 0x80a00
	s_addc_u32 s19, s89, 0
	s_add_u32 s20, s88, 0x80b00
	s_addc_u32 s21, s89, 0
	s_add_u32 s22, s88, 0x80c00
	s_addc_u32 s23, s89, 0
	s_add_u32 s24, s88, 0x80d00
	s_addc_u32 s25, s89, 0
	s_add_u32 s26, s88, 0x80e00
	s_addc_u32 s27, s89, 0
	s_add_u32 s28, s88, 0x80f00
	s_addc_u32 s29, s89, 0
	s_add_u32 s34, s88, 0x81000
	s_addc_u32 s35, s89, 0
	s_add_u32 s36, s88, 0x81100
	s_addc_u32 s37, s89, 0
	s_add_u32 s38, s88, 0x81200
	s_addc_u32 s39, s89, 0
	s_add_u32 s42, s88, 0x81300
	s_mul_i32 s31, s31, s76
	s_addc_u32 s43, s89, 0
	s_mov_b32 s33, 1
	v_mov_b32_e32 v16, 0
	s_branch .LBB0_1024
